# speedup vs baseline: 1.0123x; 1.0022x over previous
.LBB2_9:
	v_mad_i64_i32 v[0:1], s[12:13], v110, 48, 0
	v_or_b32_e32 v0, v0, v108
	v_lshlrev_b64 v[0:1], 8, v[0:1]
	v_lshl_add_u64 v[0:1], v[114:115], 0, v[0:1]
	v_add_co_u32_e32 v2, vcc, s15, v0
	global_load_dwordx4 v[24:27], v[0:1], off
	global_load_dwordx4 v[20:23], v[0:1], off offset:64
	global_load_dwordx4 v[16:19], v[0:1], off offset:128
	global_load_dwordx4 v[12:15], v[0:1], off offset:192
	v_addc_co_u32_e32 v3, vcc, 0, v1, vcc
	v_add_co_u32_e32 v0, vcc, 0x2000, v0
	v_ashrrev_i32_e32 v111, 31, v110
	s_nop 0
	v_addc_co_u32_e32 v1, vcc, 0, v1, vcc
	global_load_dwordx4 v[64:67], v[2:3], off
	global_load_dwordx4 v[56:59], v[2:3], off offset:64
	global_load_dwordx4 v[40:43], v[2:3], off offset:128
	global_load_dwordx4 v[28:31], v[2:3], off offset:192
	global_load_dwordx4 v[68:71], v[0:1], off
	global_load_dwordx4 v[60:63], v[0:1], off offset:64
	global_load_dwordx4 v[44:47], v[0:1], off offset:128
	global_load_dwordx4 v[32:35], v[0:1], off offset:192
	s_mov_b32 s12, 11
	v_mov_b32_e32 v72, v116
	s_mov_b32 s13, 0
	v_mov_b32_e32 v73, v109
	v_add_u32_e32 v121, v109, v112
	v_add_u32_e32 v122, 0x1f200, v112
	v_add_u32_e32 v124, v116, v112
	v_add_u32_e32 v124, 0x17600, v124
	v_mov_b32_e32 v0, 0
	v_mov_b32_e32 v1, v113
	v_mov_b32_e32 v2, v113
	v_mov_b32_e32 v3, v113
	v_mov_b32_e32 v36, 0
	v_mov_b32_e32 v37, v113
	v_mov_b32_e32 v38, v113
	v_mov_b32_e32 v39, v113
	v_mov_b32_e32 v48, 0
	v_mov_b32_e32 v49, v113
	v_mov_b32_e32 v50, v113
	v_mov_b32_e32 v51, v113
	v_mov_b32_e32 v52, 0
	v_mov_b32_e32 v53, v113
	v_mov_b32_e32 v54, v113
	v_mov_b32_e32 v55, v113
	v_mov_b32_e32 v4, 0
	v_mov_b32_e32 v5, v113
	v_mov_b32_e32 v6, v113
	v_mov_b32_e32 v7, v113
	v_mov_b32_e32 v8, 0
	v_mov_b32_e32 v9, v113
	v_mov_b32_e32 v10, v113
	v_mov_b32_e32 v11, v113
